# baseline (speedup 1.0000x reference)
_Z14rnn_b4s_kernelPKfS0_S0_S0_S0_S0_S0_Pf:
	s_load_dwordx8 s[12:19], s[0:1], 0x0
	s_load_dwordx8 s[4:11], s[0:1], 0x20
	v_readfirstlane_b32 s0, v0
	s_lshr_b32 s24, s0, 6
	s_lshl_b32 s0, s2, 5
	s_and_b32 s0, s0, 0xe0
	s_lshr_b32 s1, s2, 3
	s_add_i32 s0, s0, s1
	s_lshl_b32 s0, s0, 4
	s_lshl_b32 s1, s24, 2
	s_mov_b32 s23, 0
	s_add_i32 s20, s1, s0
	s_mov_b32 s21, s23
	s_lshl_b64 s[0:1], s[20:21], 15
	v_and_b32_e32 v174, 63, v0
	s_mulk_i32 s24, 0x4400
	s_waitcnt lgkmcnt(0)
	s_add_u32 s0, s12, s0
	s_addc_u32 s1, s13, s1
	v_lshlrev_b32_e32 v2, 4, v174
	v_mov_b32_e32 v3, 0
	s_mov_b32 m0, s24
	v_and_b32_e32 v64, 1, v0
	v_and_b32_e32 v18, 2, v0
	v_lshl_add_u64 v[166:167], s[0:1], 0, v[2:3]
	global_load_lds_dwordx4 v2, s[0:1] nt
	v_lshlrev_b32_e32 v4, 6, v64
	v_and_b32_e32 v2, 48, v0
	v_lshlrev_b32_e32 v12, 2, v18
	v_lshlrev_b32_e32 v66, 1, v0
	v_and_b32_e32 v1, 15, v0
	v_or3_b32 v65, v4, v12, v2
	v_and_b32_e32 v4, 32, v66
	v_mov_b32_e32 v5, v3
	v_lshl_add_u64 v[14:15], s[14:15], 0, v[4:5]
	v_lshlrev_b32_e32 v4, 6, v1
	v_lshl_add_u64 v[16:17], v[14:15], 0, v[4:5]
	v_add_u32_e32 v18, -1, v18
	v_lshl_add_u64 v[20:21], s[16:17], 0, v[2:3]
	global_load_dwordx4 v[4:7], v[16:17], off offset:16
	global_load_dwordx4 v[8:11], v[16:17], off
	v_lshlrev_b32_e32 v16, 7, v1
	v_mov_b32_e32 v17, v3
	v_bitop3_b32 v19, v0, 2, v0 bitop3:0xc
	v_and_b32_e32 v18, 2, v18
	v_lshl_add_u64 v[16:17], v[20:21], 0, v[16:17]
	v_mov_b32_e32 v13, v3
	v_lshlrev_b32_e32 v22, 2, v19
	v_mov_b32_e32 v23, v3
	v_lshlrev_b32_e32 v26, 2, v18
	v_mov_b32_e32 v27, v3
	v_or_b32_e32 v1, 16, v1
	v_lshl_add_u64 v[24:25], v[16:17], 0, v[12:13]
	v_lshl_add_u64 v[46:47], v[16:17], 0, v[22:23]
	v_lshl_add_u64 v[48:49], v[16:17], 0, v[26:27]
	v_lshlrev_b32_e32 v16, 6, v1
	v_mov_b32_e32 v17, v3
	v_lshl_add_u64 v[14:15], v[14:15], 0, v[16:17]
	global_load_dwordx4 v[16:19], v[14:15], off offset:16
	global_load_dwordx4 v[42:45], v[14:15], off
	v_lshlrev_b32_e32 v14, 7, v1
	v_mov_b32_e32 v15, v3
	v_lshl_add_u64 v[14:15], v[20:21], 0, v[14:15]
	v_lshl_add_u64 v[12:13], v[14:15], 0, v[12:13]
	v_lshl_add_u64 v[50:51], v[14:15], 0, v[22:23]
	v_lshl_add_u64 v[14:15], v[14:15], 0, v[26:27]
	global_load_dwordx2 v[168:169], v65, s[6:7] offset:128
	global_load_dwordx2 v[170:171], v65, s[6:7]
	global_load_dwordx2 v[20:21], v[12:13], off
	global_load_dwordx2 v[22:23], v[14:15], off offset:64
	global_load_dwordx2 v[52:53], v[50:51], off
	global_load_dwordx2 v[54:55], v[12:13], off offset:64
	global_load_dwordx2 v[56:57], v[48:49], off offset:64
	global_load_dwordx2 v[58:59], v[46:47], off
	global_load_dwordx2 v[60:61], v[24:25], off offset:64
	global_load_dwordx2 v[62:63], v[24:25], off
	global_load_dwordx4 v[26:29], v2, s[4:5] offset:64
	global_load_dwordx4 v[34:37], v2, s[4:5]
	global_load_dwordx4 v[30:33], v2, s[18:19] offset:64
	global_load_dwordx4 v[38:41], v2, s[18:19]
	s_mov_b64 s[0:1], 0x8000
	v_lshl_add_u64 v[2:3], v[166:167], 0, s[0:1]
	s_add_i32 m0, s24, 0x440
	s_mov_b64 s[0:1], 0x10000
	global_load_lds_dwordx4 v[2:3], off nt
	v_lshl_add_u64 v[2:3], v[166:167], 0, s[0:1]
	s_add_i32 m0, s24, 0x880
	s_mov_b64 s[0:1], 0x18000
	global_load_lds_dwordx4 v[2:3], off nt
	v_lshl_add_u64 v[2:3], v[166:167], 0, s[0:1]
	s_add_i32 m0, s24, 0xcc0
	s_mov_b64 s[0:1], 0x400
	s_load_dwordx2 s[2:3], s[8:9], 0x0
	global_load_lds_dwordx4 v[2:3], off nt
	s_add_i32 m0, s24, 0x1100
	v_lshl_add_u64 v[2:3], v[166:167], 0, s[0:1]
	s_mov_b64 s[0:1], 0x8400
	global_load_lds_dwordx4 v[2:3], off nt
	v_lshl_add_u64 v[2:3], v[166:167], 0, s[0:1]
	s_add_i32 m0, s24, 0x1540
	s_mov_b64 s[0:1], 0x10400
	global_load_lds_dwordx4 v[2:3], off nt
	v_lshl_add_u64 v[2:3], v[166:167], 0, s[0:1]
	s_add_i32 m0, s24, 0x1980
	s_mov_b64 s[0:1], 0x18400
	global_load_lds_dwordx4 v[2:3], off nt
	v_lshl_add_u64 v[2:3], v[166:167], 0, s[0:1]
	s_add_i32 m0, s24, 0x1dc0
	global_load_lds_dwordx4 v[2:3], off nt
	s_mov_b64 s[0:1], 0x800
	s_add_i32 m0, s24, 0x2200
	v_lshl_add_u64 v[2:3], v[166:167], 0, s[0:1]
	global_load_lds_dwordx4 v[2:3], off nt
	s_mov_b64 s[0:1], 0x8800
	s_add_i32 m0, s24, 0x2640
	v_lshl_add_u64 v[2:3], v[166:167], 0, s[0:1]
	global_load_lds_dwordx4 v[2:3], off nt
	s_mov_b64 s[0:1], 0x10800
	s_add_i32 m0, s24, 0x2a80
	v_lshl_add_u64 v[2:3], v[166:167], 0, s[0:1]
	global_load_lds_dwordx4 v[2:3], off nt
	s_mov_b64 s[0:1], 0x18800
	s_add_i32 m0, s24, 0x2ec0
	v_lshl_add_u64 v[2:3], v[166:167], 0, s[0:1]
	global_load_lds_dwordx4 v[2:3], off nt
	s_mov_b64 s[0:1], 0xc00
	s_add_i32 m0, s24, 0x3300
	v_lshl_add_u64 v[2:3], v[166:167], 0, s[0:1]
	global_load_lds_dwordx4 v[2:3], off nt
	s_mov_b64 s[0:1], 0x8c00
	s_add_i32 m0, s24, 0x3740
	v_lshl_add_u64 v[2:3], v[166:167], 0, s[0:1]
	global_load_lds_dwordx4 v[2:3], off nt
	s_mov_b64 s[0:1], 0x10c00
	s_add_i32 m0, s24, 0x3b80
	v_lshl_add_u64 v[2:3], v[166:167], 0, s[0:1]
	global_load_lds_dwordx4 v[2:3], off nt
	s_mov_b64 s[0:1], 0x18c00
	s_add_i32 m0, s24, 0x3fc0
	v_lshl_add_u64 v[2:3], v[166:167], 0, s[0:1]
	global_load_lds_dwordx4 v[2:3], off nt
	s_waitcnt lgkmcnt(0)
	v_mov_b64_e32 v[172:173], s[2:3]
	s_mov_b32 s2, 0x4038aa3b
	s_waitcnt vmcnt(15)
	s_waitcnt vmcnt(15)
	s_nop 0
	v_fma_mixlo_f16 v2, v8, s2, 0
	v_cmp_gt_u32_e64 s[0:1], 32, v174
	v_cmp_lt_u32_e32 vcc, 31, v174
	s_movk_i32 s5, 0x440
	v_cndmask_b32_e64 v12, 0, v2, s[0:1]
	v_cndmask_b32_e32 v14, 0, v2, vcc
	v_fma_mixlo_f16 v2, v9, s2, 0
	s_mov_b32 s4, 0xc0b8aa3b
	v_cndmask_b32_e64 v13, 0, v2, s[0:1]
	v_cndmask_b32_e32 v15, 0, v2, vcc
	v_pk_mov_b32 v[2:3], v[62:63], v[60:61] op_sel:[1,0]
	v_fma_mixlo_f16 v4, v4, s2, 0
	v_pk_mul_f32 v[2:3], v[2:3], s[4:5] op_sel_hi:[1,0]
	v_fma_mixlo_f16 v8, v11, s2, 0
	v_cndmask_b32_e64 v25, 0, v4, s[0:1]
	v_cndmask_b32_e32 v46, 0, v4, vcc
	v_fma_mixlo_f16 v4, v5, s2, 0
	v_fma_mixlo_f16 v1, v62, s4, 0
	v_cvt_pk_f16_f32 v3, v2, v3
	v_cndmask_b32_e64 v11, 0, v8, s[0:1]
	v_cndmask_b32_e32 v24, 0, v8, vcc
	v_pk_mov_b32 v[8:9], v[60:61], v[58:59] op_sel:[1,0]
	v_cndmask_b32_e64 v47, 0, v4, s[0:1]
	v_cndmask_b32_e32 v48, 0, v4, vcc
	v_pk_mov_b32 v[4:5], v[58:59], v[56:57] op_sel:[1,0]
	v_pack_b32_f16 v2, v1, v3
	v_fma_mixlo_f16 v1, v10, s2, 0
	v_pk_mul_f32 v[8:9], v[8:9], s[4:5] op_sel_hi:[1,0]
	v_pk_mul_f32 v[4:5], v[4:5], s[4:5] op_sel_hi:[1,0]
	v_cndmask_b32_e64 v10, 0, v1, s[0:1]
	v_cvt_pk_f16_f32 v8, v8, v9
	v_cvt_pk_f16_f32 v5, v4, v5
	v_fma_mixlo_f16 v6, v6, s2, 0
	v_fma_mixlo_f16 v50, v7, s2, 0
	v_alignbit_b32 v3, v8, v3, 16
	v_alignbit_b32 v4, v5, v8, 16
	v_cndmask_b32_e64 v8, 0, v6, s[0:1]
	v_cndmask_b32_e32 v49, 0, v6, vcc
	v_cndmask_b32_e64 v6, 0, v50, s[0:1]
	v_pack_b32_f16 v7, v10, v11
	v_cndmask_b32_e32 v10, 0, v50, vcc
	v_pack_b32_f16 v9, v8, v6
	v_pack_b32_f16 v6, v12, v13
	v_pack_b32_f16 v13, v49, v10
	v_pack_b32_f16 v10, v14, v15
	v_fma_mixlo_f16 v14, v42, s2, 0
	v_pack_b32_f16 v8, v25, v47
	v_pack_b32_f16 v12, v46, v48
	v_cndmask_b32_e64 v46, 0, v14, s[0:1]
	v_cndmask_b32_e32 v47, 0, v14, vcc
	v_fma_mixlo_f16 v14, v43, s2, 0
	v_cndmask_b32_e32 v1, 0, v1, vcc
	v_pack_b32_f16 v11, v1, v24
	v_fma_mixlo_f16 v24, v45, s2, 0
	v_cndmask_b32_e64 v45, 0, v24, s[0:1]
	v_cndmask_b32_e32 v50, 0, v24, vcc
	v_pk_mov_b32 v[24:25], v[52:53], v[22:23] op_sel:[1,0]
	v_fma_mixlo_f16 v16, v16, s2, 0
	v_pk_mul_f32 v[24:25], v[24:25], s[4:5] op_sel_hi:[1,0]
	v_lshrrev_b32_e32 v5, 16, v5
	v_cvt_pk_f16_f32 v24, v24, v25
	v_cndmask_b32_e64 v25, 0, v16, s[0:1]
	v_cndmask_b32_e32 v42, 0, v16, vcc
	v_fma_mixlo_f16 v16, v17, s2, 0
	v_fma_mixhi_f16 v5, v57, s4, 0
	v_cndmask_b32_e64 v43, 0, v16, s[0:1]
	v_cndmask_b32_e32 v51, 0, v16, vcc
	v_pk_mov_b32 v[16:17], v[22:23], v[20:21] op_sel:[1,0]
	v_cndmask_b32_e64 v48, 0, v14, s[0:1]
	v_cndmask_b32_e32 v49, 0, v14, vcc
	v_pk_mov_b32 v[14:15], v[54:55], v[52:53] op_sel:[1,0]
	v_pk_mul_f32 v[16:17], v[16:17], s[4:5] op_sel_hi:[1,0]
	s_mov_b32 s12, 0xb800b800
	v_pk_mul_f32 v[14:15], v[14:15], s[4:5] op_sel_hi:[1,0]
	v_cvt_pk_f16_f32 v17, v16, v17
	s_mov_b32 s14, s12
	s_mov_b32 s15, s12
	v_fma_mixlo_f16 v1, v54, s4, 0
	v_cvt_pk_f16_f32 v15, v14, v15
	v_alignbit_b32 v16, v17, v24, 16
	v_lshrrev_b32_e32 v17, 16, v17
	v_pk_add_f32 v[36:37], v[40:41], v[36:37]
	v_pk_add_f32 v[34:35], v[38:39], v[34:35]
	s_mov_b32 s13, s12
	v_mov_b64_e32 v[40:41], s[14:15]
	v_pack_b32_f16 v14, v1, v15
	v_alignbit_b32 v15, v24, v15, 16
	v_fma_mixhi_f16 v17, v21, s4, 0
	v_pk_mul_f32 v[36:37], v[36:37], s[2:3] op_sel_hi:[1,0]
	v_pk_mul_f32 v[34:35], v[34:35], s[2:3] op_sel_hi:[1,0]
	v_mov_b64_e32 v[38:39], s[12:13]
	v_fma_mixlo_f16 v1, v44, s2, 0
	v_fma_mixlo_f16 v18, v18, s2, 0
	v_mfma_f32_16x16x32_f16 v[34:37], v[2:5], v[38:41], v[34:37]
	v_fma_mixlo_f16 v23, v19, s2, 0
	v_and_b32_e32 v176, 3, v0
	v_cndmask_b32_e64 v44, 0, v1, s[0:1]
	v_cndmask_b32_e32 v1, 0, v1, vcc
	v_cndmask_b32_e64 v20, 0, v18, s[0:1]
	v_cndmask_b32_e32 v22, 0, v18, vcc
	v_cndmask_b32_e64 v18, 0, v23, s[0:1]
	v_cndmask_b32_e32 v23, 0, v23, vcc
	v_pk_add_f32 v[28:29], v[32:33], v[28:29]
	v_pk_add_f32 v[26:27], v[30:31], v[26:27]
	v_cmp_gt_u32_e32 vcc, 2, v176
	v_cmp_eq_u32_e64 s[0:1], 0, v64
	v_bfe_u32 v175, v0, 2, 2
	v_pack_b32_f16 v21, v20, v18
	v_pack_b32_f16 v20, v25, v43
	v_pack_b32_f16 v25, v22, v23
	v_pack_b32_f16 v23, v1, v50
	v_pk_mul_f32 v[28:29], v[28:29], s[2:3] op_sel_hi:[1,0]
	v_pk_mul_f32 v[26:27], v[26:27], s[2:3] op_sel_hi:[1,0]
	v_mov_b32_e32 v1, 0xf149f2ca
	s_and_b64 s[2:3], s[0:1], vcc
	v_bitop3_b32 v0, v0, 2, 3 bitop3:0x6c
	v_mfma_f32_16x16x32_f16 v[30:33], v[14:17], v[38:41], v[26:29]
	v_pack_b32_f16 v19, v44, v45
	v_pack_b32_f16 v18, v46, v48
	v_pack_b32_f16 v24, v42, v51
	v_cndmask_b32_e64 v26, v1, v34, s[2:3]
	v_cndmask_b32_e64 v27, v1, v35, s[2:3]
	v_cmp_gt_u32_e64 s[2:3], 2, v0
	s_and_b64 s[0:1], s[0:1], s[2:3]
	v_cndmask_b32_e64 v28, v1, v36, s[0:1]
	v_cndmask_b32_e64 v29, v1, v37, s[0:1]
	v_cmp_eq_u32_e64 s[0:1], 1, v64
	s_and_b64 vcc, s[0:1], vcc
	v_and_b32_e32 v0, 0x60, v66
	v_cndmask_b32_e32 v30, v1, v30, vcc
	v_cndmask_b32_e32 v31, v1, v31, vcc
	s_and_b64 vcc, s[0:1], s[2:3]
	v_or_b32_e32 v0, s24, v0
	v_mov_b32_e32 v34, 0x38003800
	v_pack_b32_f16 v22, v47, v49
	v_cndmask_b32_e32 v32, v1, v32, vcc
	v_cndmask_b32_e32 v33, v1, v33, vcc
	v_mad_u32_u24 v177, v175, s5, v0
	s_mov_b64 s[0:1], 0x1000
	s_mov_b64 s[2:3], 0x9000
	s_mov_b64 s[4:5], 0x11000
	s_mov_b64 s[6:7], 0x19000
	s_mov_b32 s8, 0
	v_mov_b32_e32 v35, v34
	v_mov_b32_e32 v37, v34
	v_mov_b32_e32 v36, v34
	v_mov_b32_e32 v94, v177
	s_waitcnt vmcnt(12)
	ds_read_b128 v[82:85], v177
	ds_read_b128 v[86:89], v177 offset:16
	s_waitcnt lgkmcnt(0)
	v_cvt_pk_f16_f32 v78, v82, v83
	v_cvt_pk_f16_f32 v79, v84, v85
	v_cvt_pk_f16_f32 v80, v86, v87
	v_cvt_pk_f16_f32 v81, v88, v89
	ds_read_b128 v[82:85], v177 offset:128
	ds_read_b128 v[86:89], v177 offset:144
	v_mfma_f32_16x16x32_f16 v[46:49], v[6:9], v[78:81], v[26:29]
	v_mfma_f32_16x16x32_f16 v[50:53], v[18:21], v[78:81], v[30:33]
	v_mfma_f32_16x16x32_f16 v[54:57], v[10:13], v[78:81], v[26:29]
	v_mfma_f32_16x16x32_f16 v[58:61], v[22:25], v[78:81], v[30:33]
	s_waitcnt lgkmcnt(0)
	v_cvt_pk_f16_f32 v78, v82, v83
	v_cvt_pk_f16_f32 v79, v84, v85
	v_cvt_pk_f16_f32 v80, v86, v87
	v_cvt_pk_f16_f32 v81, v88, v89
	s_nop 1
	.p2align 6
